# speedup vs baseline: 1.0061x; 1.0061x over previous
	.text
	.protected	_Z13attn11_kernelILi4EEvPc
	.globl	_Z13attn11_kernelILi4EEvPc
	.p2align	8
	.type	_Z13attn11_kernelILi4EEvPc,@function

.LBB3_4:
	v_add_u32_e32 v112, s38, v193
	v_add_u32_e32 v114, s33, v193
	v_readfirstlane_b32 s34, v112
	v_add_u32_e32 v114, 0x6000, v114
	s_mov_b32 m0, s34
	v_readfirstlane_b32 s34, v114
	global_load_lds_dwordx4 v[188:189], off
	v_lshl_add_u64 v[112:113], v[190:191], 0, s[18:19]
	s_mov_b32 m0, s34
	s_add_i32 s34, s3, 0
	global_load_lds_dwordx4 v[112:113], off
	v_add_u32_e32 v112, s34, v199
	v_add_u32_e32 v205, v112, v195
	v_add_u32_e32 v206, v112, v200
	ds_read_b128 v[112:115], v205
	ds_read_b128 v[128:131], v205 offset:2048
	ds_read_b128 v[116:119], v206
	ds_read_b128 v[132:135], v206 offset:2048
	s_setprio 1
	v_exp_f32_e32 v80, v80
	v_exp_f32_e32 v81, v81
	v_exp_f32_e32 v82, v82
	v_exp_f32_e32 v83, v83
	v_exp_f32_e32 v84, v84
	v_exp_f32_e32 v85, v85
	v_exp_f32_e32 v86, v86
	v_exp_f32_e32 v87, v87
	s_add_i32 s35, s38, 0
	s_waitcnt lgkmcnt(0)
	v_mfma_scale_f32_32x32x64_f8f6f4 v[112:127], v[112:119], v[152:159], v[64:79], v173, v194 op_sel_hi:[0,0,0]
	v_cvt_pk_fp8_f32 v160, v80, v81
	v_cvt_pk_fp8_f32 v161, v84, v85
	v_exp_f32_e32 v88, v88
	v_exp_f32_e32 v89, v89
	v_cvt_pk_fp8_f32 v160, v82, v83 op_sel:[0,0,1]
	v_cvt_pk_fp8_f32 v161, v86, v87 op_sel:[0,0,1]
	v_exp_f32_e32 v90, v90
	v_exp_f32_e32 v91, v91
	v_exp_f32_e32 v92, v92
	v_exp_f32_e32 v93, v93
	v_exp_f32_e32 v94, v94
	v_exp_f32_e32 v95, v95
	s_setprio 0
	v_add_u32_e32 v80, s35, v199
	v_add_u32_e32 v210, v80, v195
	v_add_u32_e32 v211, v80, v200
	ds_read_b128 v[80:83], v210 offset:24576
	ds_read_b128 v[212:215], v210 offset:26624
	ds_read_b128 v[84:87], v211 offset:24576
	ds_read_b128 v[216:219], v211 offset:26624
	v_cvt_pk_fp8_f32 v162, v88, v89
	v_cvt_pk_fp8_f32 v163, v92, v93
	v_exp_f32_e32 v96, v96
	v_exp_f32_e32 v97, v97
	v_cvt_pk_fp8_f32 v162, v90, v91 op_sel:[0,0,1]
	v_cvt_pk_fp8_f32 v163, v94, v95 op_sel:[0,0,1]
	v_exp_f32_e32 v98, v98
	v_exp_f32_e32 v99, v99
	v_exp_f32_e32 v100, v100
	v_exp_f32_e32 v101, v101
	v_exp_f32_e32 v102, v102
	v_exp_f32_e32 v103, v103
	v_mfma_scale_f32_32x32x64_f8f6f4 v[128:143], v[128:135], v[152:159], v[64:79], v173, v194 op_sel_hi:[0,0,0]
	v_cvt_pk_fp8_f32 v164, v96, v97
	v_cvt_pk_fp8_f32 v165, v100, v101
	v_exp_f32_e32 v104, v104
	v_exp_f32_e32 v105, v105
	v_cvt_pk_fp8_f32 v164, v98, v99 op_sel:[0,0,1]
	v_cvt_pk_fp8_f32 v165, v102, v103 op_sel:[0,0,1]
	v_exp_f32_e32 v106, v106
	v_exp_f32_e32 v107, v107
	v_exp_f32_e32 v108, v108
	v_exp_f32_e32 v109, v109
	v_exp_f32_e32 v110, v110
	v_exp_f32_e32 v111, v111
	s_nop 0
	v_cvt_pk_fp8_f32 v166, v104, v105
	v_cvt_pk_fp8_f32 v167, v108, v109
	v_cvt_pk_fp8_f32 v166, v106, v107 op_sel:[0,0,1]
	v_cvt_pk_fp8_f32 v167, v110, v111 op_sel:[0,0,1]
	s_setprio 1
	s_waitcnt lgkmcnt(0)
	v_mfma_scale_f32_32x32x64_f8f6f4 v[32:47], v[80:87], v[160:167], v[32:47], v194, v194 op_sel_hi:[0,0,0]
	v_max3_f32 v88, v112, s5, v113
	v_max3_f32 v88, v88, v114, v115
	v_max3_f32 v88, v88, v116, v117
	v_max3_f32 v88, v88, v118, v119
	v_max3_f32 v88, v88, v120, v121
	v_max3_f32 v88, v88, v122, v123
	v_max3_f32 v88, v88, v124, v125
	v_max3_f32 v88, v88, v126, v127
	v_mfma_scale_f32_32x32x64_f8f6f4 v[16:31], v[212:219], v[160:167], v[16:31], v194, v194 op_sel_hi:[0,0,0]
	v_max3_f32 v80, v128, s5, v129
	v_max3_f32 v80, v80, v130, v131
	v_max3_f32 v80, v80, v132, v133
	v_max3_f32 v80, v80, v134, v135
	v_max3_f32 v80, v80, v136, v137
	v_max3_f32 v80, v80, v138, v139
	v_max3_f32 v80, v80, v140, v141
	v_max3_f32 v80, v80, v142, v143
	v_mfma_scale_f32_32x32x64_f8f6f4 v[48:63], v[144:151], v[160:167], v[48:63], v194, v194 op_sel_hi:[0,0,0]
	s_setprio 0
	v_max_f32_e32 v80, v88, v80
	v_cmp_lt_f32_e32 vcc, s36, v80
	s_cbranch_vccnz .LBB3_8
.LBB3_5:
	s_waitcnt vmcnt(2) lgkmcnt(0)
	s_barrier
	v_add_u32_e32 v207, s34, v169
	v_add_u32_e32 v209, s35, v169
	v_readfirstlane_b32 s34, v207
	v_add_u32_e32 v208, 0x6000, v209
	v_lshl_add_u64 v[80:81], v[188:189], 0, s[8:9]
	s_mov_b32 m0, s34
	v_readfirstlane_b32 s34, v208
	global_load_lds_dwordx4 v[80:81], off
	s_mov_b32 m0, s34
	s_add_i32 s34, s33, 0
	global_load_lds_dwordx4 v[190:191], off
	v_add_u32_e32 v80, s34, v199
	v_add_u32_e32 v203, v80, v195
	v_add_u32_e32 v204, v80, v200
	ds_read_b128 v[80:83], v203
	ds_read_b128 v[96:99], v203 offset:2048
	ds_read_b128 v[84:87], v204
	ds_read_b128 v[100:103], v204 offset:2048
	s_setprio 1
	v_exp_f32_e32 v112, v112
	v_exp_f32_e32 v113, v113
	v_exp_f32_e32 v114, v114
	v_exp_f32_e32 v115, v115
	v_exp_f32_e32 v116, v116
	v_exp_f32_e32 v117, v117
	v_exp_f32_e32 v118, v118
	v_exp_f32_e32 v119, v119
	s_waitcnt lgkmcnt(0)
	v_mfma_scale_f32_32x32x64_f8f6f4 v[80:95], v[80:87], v[152:159], v[64:79], v173, v194 op_sel_hi:[0,0,0]
	v_cvt_pk_fp8_f32 v160, v112, v113
	v_cvt_pk_fp8_f32 v161, v116, v117
	v_exp_f32_e32 v120, v120
	v_exp_f32_e32 v121, v121
	v_cvt_pk_fp8_f32 v160, v114, v115 op_sel:[0,0,1]
	v_cvt_pk_fp8_f32 v161, v118, v119 op_sel:[0,0,1]
	v_exp_f32_e32 v122, v122
	v_exp_f32_e32 v123, v123
	v_exp_f32_e32 v124, v124
	v_exp_f32_e32 v125, v125
	v_exp_f32_e32 v126, v126
	v_exp_f32_e32 v127, v127
	s_setprio 0
	ds_read_b128 v[112:115], v205 offset:24576
	ds_read_b128 v[212:215], v205 offset:26624
	ds_read_b128 v[116:119], v206 offset:24576
	ds_read_b128 v[216:219], v206 offset:26624
	v_cvt_pk_fp8_f32 v162, v120, v121
	v_cvt_pk_fp8_f32 v163, v124, v125
	v_exp_f32_e32 v128, v128
	v_exp_f32_e32 v129, v129
	v_cvt_pk_fp8_f32 v162, v122, v123 op_sel:[0,0,1]
	v_cvt_pk_fp8_f32 v163, v126, v127 op_sel:[0,0,1]
	v_exp_f32_e32 v130, v130
	v_exp_f32_e32 v131, v131
	v_exp_f32_e32 v132, v132
	v_exp_f32_e32 v133, v133
	v_exp_f32_e32 v134, v134
	v_exp_f32_e32 v135, v135
	v_mfma_scale_f32_32x32x64_f8f6f4 v[96:111], v[96:103], v[152:159], v[64:79], v173, v194 op_sel_hi:[0,0,0]
	v_cvt_pk_fp8_f32 v164, v128, v129
	v_cvt_pk_fp8_f32 v165, v132, v133
	v_exp_f32_e32 v136, v136
	v_exp_f32_e32 v137, v137
	v_cvt_pk_fp8_f32 v164, v130, v131 op_sel:[0,0,1]
	v_cvt_pk_fp8_f32 v165, v134, v135 op_sel:[0,0,1]
	v_exp_f32_e32 v138, v138
	v_exp_f32_e32 v139, v139
	v_exp_f32_e32 v140, v140
	v_exp_f32_e32 v141, v141
	v_exp_f32_e32 v142, v142
	v_exp_f32_e32 v143, v143
	s_nop 0
	v_cvt_pk_fp8_f32 v166, v136, v137
	v_cvt_pk_fp8_f32 v167, v140, v141
	v_cvt_pk_fp8_f32 v166, v138, v139 op_sel:[0,0,1]
	v_cvt_pk_fp8_f32 v167, v142, v143 op_sel:[0,0,1]
	s_setprio 1
	s_waitcnt lgkmcnt(0)
	v_mfma_scale_f32_32x32x64_f8f6f4 v[32:47], v[112:119], v[160:167], v[32:47], v194, v194 op_sel_hi:[0,0,0]
	v_max3_f32 v120, v80, s5, v81
	v_max3_f32 v120, v120, v82, v83
	v_max3_f32 v120, v120, v84, v85
	v_max3_f32 v120, v120, v86, v87
	v_max3_f32 v120, v120, v88, v89
	v_max3_f32 v120, v120, v90, v91
	v_max3_f32 v120, v120, v92, v93
	v_max3_f32 v120, v120, v94, v95
	v_mfma_scale_f32_32x32x64_f8f6f4 v[16:31], v[212:219], v[160:167], v[16:31], v194, v194 op_sel_hi:[0,0,0]
	v_max3_f32 v112, v96, s5, v97
	v_max3_f32 v112, v112, v98, v99
	v_max3_f32 v112, v112, v100, v101
	v_max3_f32 v112, v112, v102, v103
	v_max3_f32 v112, v112, v104, v105
	v_max3_f32 v112, v112, v106, v107
	v_max3_f32 v112, v112, v108, v109
	v_max3_f32 v112, v112, v110, v111
	v_mfma_scale_f32_32x32x64_f8f6f4 v[48:63], v[144:151], v[160:167], v[48:63], v194, v194 op_sel_hi:[0,0,0]
	s_setprio 0
	v_max_f32_e32 v112, v120, v112
	v_cmp_lt_f32_e32 vcc, s36, v112
	s_cbranch_vccnz .LBB3_9

.LBB3_8:
	v_mov_b32_e32 v81, v80
	s_nop 1
	v_permlane32_swap_b32_e32 v80, v81
	v_max_f32_e32 v80, v80, v81
	v_max_f32_e32 v80, v80, v80
	v_max_f32_e32 v81, 0, v80
	v_exp_f32_e64 v80, -v81
	v_sub_f32_e32 v79, v79, v81
	v_sub_f32_e32 v78, v78, v81
	v_sub_f32_e32 v77, v77, v81
	v_sub_f32_e32 v76, v76, v81
	v_sub_f32_e32 v75, v75, v81
	v_sub_f32_e32 v74, v74, v81
	v_sub_f32_e32 v73, v73, v81
	v_sub_f32_e32 v72, v72, v81
	v_sub_f32_e32 v71, v71, v81
	v_sub_f32_e32 v70, v70, v81
	v_sub_f32_e32 v69, v69, v81
	v_sub_f32_e32 v68, v68, v81
	v_sub_f32_e32 v67, v67, v81
	v_sub_f32_e32 v66, v66, v81
	v_sub_f32_e32 v65, v65, v81
	v_sub_f32_e32 v64, v64, v81
	v_sub_f32_e32 v127, v127, v81
	v_sub_f32_e32 v126, v126, v81
	v_sub_f32_e32 v125, v125, v81
	v_sub_f32_e32 v124, v124, v81
	v_sub_f32_e32 v123, v123, v81
	v_sub_f32_e32 v122, v122, v81
	v_sub_f32_e32 v121, v121, v81
	v_sub_f32_e32 v120, v120, v81
	v_sub_f32_e32 v119, v119, v81
	v_sub_f32_e32 v118, v118, v81
	v_sub_f32_e32 v117, v117, v81
	v_sub_f32_e32 v116, v116, v81
	v_sub_f32_e32 v115, v115, v81
	v_sub_f32_e32 v114, v114, v81
	v_sub_f32_e32 v113, v113, v81
	v_sub_f32_e32 v112, v112, v81
	v_sub_f32_e32 v143, v143, v81
	v_sub_f32_e32 v142, v142, v81
	v_sub_f32_e32 v141, v141, v81
	v_sub_f32_e32 v140, v140, v81
	v_sub_f32_e32 v139, v139, v81
	v_sub_f32_e32 v138, v138, v81
	v_sub_f32_e32 v137, v137, v81
	v_sub_f32_e32 v136, v136, v81
	v_sub_f32_e32 v135, v135, v81
	v_sub_f32_e32 v134, v134, v81
	v_sub_f32_e32 v133, v133, v81
	v_sub_f32_e32 v132, v132, v81
	v_sub_f32_e32 v131, v131, v81
	v_sub_f32_e32 v130, v130, v81
	v_sub_f32_e32 v129, v129, v81
	v_sub_f32_e32 v128, v128, v81
	v_pk_mul_f32 v[46:47], v[80:81], v[46:47] op_sel_hi:[0,1]
	v_pk_mul_f32 v[44:45], v[80:81], v[44:45] op_sel_hi:[0,1]
	v_pk_mul_f32 v[42:43], v[80:81], v[42:43] op_sel_hi:[0,1]
	v_pk_mul_f32 v[40:41], v[80:81], v[40:41] op_sel_hi:[0,1]
	v_pk_mul_f32 v[38:39], v[80:81], v[38:39] op_sel_hi:[0,1]
	v_pk_mul_f32 v[36:37], v[80:81], v[36:37] op_sel_hi:[0,1]
	v_pk_mul_f32 v[34:35], v[80:81], v[34:35] op_sel_hi:[0,1]
	v_pk_mul_f32 v[32:33], v[80:81], v[32:33] op_sel_hi:[0,1]
	v_pk_mul_f32 v[30:31], v[80:81], v[30:31] op_sel_hi:[0,1]
	v_pk_mul_f32 v[28:29], v[80:81], v[28:29] op_sel_hi:[0,1]
	v_pk_mul_f32 v[26:27], v[80:81], v[26:27] op_sel_hi:[0,1]
	v_pk_mul_f32 v[24:25], v[80:81], v[24:25] op_sel_hi:[0,1]
	v_pk_mul_f32 v[22:23], v[80:81], v[22:23] op_sel_hi:[0,1]
	v_pk_mul_f32 v[20:21], v[80:81], v[20:21] op_sel_hi:[0,1]
	v_pk_mul_f32 v[18:19], v[80:81], v[18:19] op_sel_hi:[0,1]
	v_pk_mul_f32 v[16:17], v[80:81], v[16:17] op_sel_hi:[0,1]
	v_pk_mul_f32 v[62:63], v[80:81], v[62:63] op_sel_hi:[0,1]
	v_pk_mul_f32 v[60:61], v[80:81], v[60:61] op_sel_hi:[0,1]
	v_pk_mul_f32 v[58:59], v[80:81], v[58:59] op_sel_hi:[0,1]
	v_pk_mul_f32 v[56:57], v[80:81], v[56:57] op_sel_hi:[0,1]
	v_pk_mul_f32 v[54:55], v[80:81], v[54:55] op_sel_hi:[0,1]
	v_pk_mul_f32 v[52:53], v[80:81], v[52:53] op_sel_hi:[0,1]
	v_pk_mul_f32 v[50:51], v[80:81], v[50:51] op_sel_hi:[0,1]
	v_pk_mul_f32 v[48:49], v[80:81], v[48:49] op_sel_hi:[0,1]
	s_branch .LBB3_5
.LBB3_9:
	v_mov_b32_e32 v113, v112
	s_nop 1
	v_permlane32_swap_b32_e32 v112, v113
	v_max_f32_e32 v112, v112, v113
	v_max_f32_e32 v112, v112, v112
	v_max_f32_e32 v113, 0, v112
	v_exp_f32_e64 v112, -v113
	v_sub_f32_e32 v79, v79, v113
	v_sub_f32_e32 v78, v78, v113
	v_sub_f32_e32 v77, v77, v113
	v_sub_f32_e32 v76, v76, v113
	v_sub_f32_e32 v75, v75, v113
	v_sub_f32_e32 v74, v74, v113
	v_sub_f32_e32 v73, v73, v113
	v_sub_f32_e32 v72, v72, v113
	v_sub_f32_e32 v71, v71, v113
	v_sub_f32_e32 v70, v70, v113
	v_sub_f32_e32 v69, v69, v113
	v_sub_f32_e32 v68, v68, v113
	v_sub_f32_e32 v67, v67, v113
	v_sub_f32_e32 v66, v66, v113
	v_sub_f32_e32 v65, v65, v113
	v_sub_f32_e32 v64, v64, v113
	v_sub_f32_e32 v95, v95, v113
	v_sub_f32_e32 v94, v94, v113
	v_sub_f32_e32 v93, v93, v113
	v_sub_f32_e32 v92, v92, v113
	v_sub_f32_e32 v91, v91, v113
	v_sub_f32_e32 v90, v90, v113
	v_sub_f32_e32 v89, v89, v113
	v_sub_f32_e32 v88, v88, v113
	v_sub_f32_e32 v87, v87, v113
	v_sub_f32_e32 v86, v86, v113
	v_sub_f32_e32 v85, v85, v113
	v_sub_f32_e32 v84, v84, v113
	v_sub_f32_e32 v83, v83, v113
	v_sub_f32_e32 v82, v82, v113
	v_sub_f32_e32 v81, v81, v113
	v_sub_f32_e32 v80, v80, v113
	v_sub_f32_e32 v111, v111, v113
	v_sub_f32_e32 v110, v110, v113
	v_sub_f32_e32 v109, v109, v113
	v_sub_f32_e32 v108, v108, v113
	v_sub_f32_e32 v107, v107, v113
	v_sub_f32_e32 v106, v106, v113
	v_sub_f32_e32 v105, v105, v113
	v_sub_f32_e32 v104, v104, v113
	v_sub_f32_e32 v103, v103, v113
	v_sub_f32_e32 v102, v102, v113
	v_sub_f32_e32 v101, v101, v113
	v_sub_f32_e32 v100, v100, v113
	v_sub_f32_e32 v99, v99, v113
	v_sub_f32_e32 v98, v98, v113
	v_sub_f32_e32 v97, v97, v113
	v_sub_f32_e32 v96, v96, v113
	v_pk_mul_f32 v[46:47], v[112:113], v[46:47] op_sel_hi:[0,1]
	v_pk_mul_f32 v[44:45], v[112:113], v[44:45] op_sel_hi:[0,1]
	v_pk_mul_f32 v[42:43], v[112:113], v[42:43] op_sel_hi:[0,1]
	v_pk_mul_f32 v[40:41], v[112:113], v[40:41] op_sel_hi:[0,1]
	v_pk_mul_f32 v[38:39], v[112:113], v[38:39] op_sel_hi:[0,1]
	v_pk_mul_f32 v[36:37], v[112:113], v[36:37] op_sel_hi:[0,1]
	v_pk_mul_f32 v[34:35], v[112:113], v[34:35] op_sel_hi:[0,1]
	v_pk_mul_f32 v[32:33], v[112:113], v[32:33] op_sel_hi:[0,1]
	v_pk_mul_f32 v[30:31], v[112:113], v[30:31] op_sel_hi:[0,1]
	v_pk_mul_f32 v[28:29], v[112:113], v[28:29] op_sel_hi:[0,1]
	v_pk_mul_f32 v[26:27], v[112:113], v[26:27] op_sel_hi:[0,1]
	v_pk_mul_f32 v[24:25], v[112:113], v[24:25] op_sel_hi:[0,1]
	v_pk_mul_f32 v[22:23], v[112:113], v[22:23] op_sel_hi:[0,1]
	v_pk_mul_f32 v[20:21], v[112:113], v[20:21] op_sel_hi:[0,1]
	v_pk_mul_f32 v[18:19], v[112:113], v[18:19] op_sel_hi:[0,1]
	v_pk_mul_f32 v[16:17], v[112:113], v[16:17] op_sel_hi:[0,1]
	v_pk_mul_f32 v[62:63], v[112:113], v[62:63] op_sel_hi:[0,1]
	v_pk_mul_f32 v[60:61], v[112:113], v[60:61] op_sel_hi:[0,1]
	v_pk_mul_f32 v[58:59], v[112:113], v[58:59] op_sel_hi:[0,1]
	v_pk_mul_f32 v[56:57], v[112:113], v[56:57] op_sel_hi:[0,1]
	v_pk_mul_f32 v[54:55], v[112:113], v[54:55] op_sel_hi:[0,1]
	v_pk_mul_f32 v[52:53], v[112:113], v[52:53] op_sel_hi:[0,1]
	v_pk_mul_f32 v[50:51], v[112:113], v[50:51] op_sel_hi:[0,1]
	v_pk_mul_f32 v[48:49], v[112:113], v[48:49] op_sel_hi:[0,1]
	s_branch .LBB3_6
.LBB3_10:
	v_add_u32_e32 v188, s34, v169
	v_add_u32_e32 v189, 0x6000, v207
	v_readfirstlane_b32 s6, v188
	v_lshl_add_u64 v[112:113], v[174:175], 0, s[22:23]
	s_mov_b32 m0, s6
	v_readfirstlane_b32 s6, v189
	global_load_lds_dwordx4 v[112:113], off
	v_lshl_add_u64 v[112:113], v[176:177], 0, s[24:25]
	s_mov_b32 m0, s6
	s_nop 0
	global_load_lds_dwordx4 v[112:113], off
	ds_read_b128 v[112:115], v210
	ds_read_b128 v[128:131], v210 offset:2048
	ds_read_b128 v[116:119], v211
	ds_read_b128 v[132:135], v211 offset:2048
	s_setprio 1
	v_exp_f32_e32 v80, v80
	v_exp_f32_e32 v81, v81
	v_exp_f32_e32 v82, v82
	v_exp_f32_e32 v83, v83
	v_exp_f32_e32 v84, v84
	v_exp_f32_e32 v85, v85
	v_exp_f32_e32 v86, v86
	v_exp_f32_e32 v87, v87
	s_waitcnt lgkmcnt(0)
	v_mfma_scale_f32_32x32x64_f8f6f4 v[112:127], v[112:119], v[152:159], v[64:79], v173, v194 op_sel_hi:[0,0,0]
	v_cvt_pk_fp8_f32 v160, v80, v81
	v_cvt_pk_fp8_f32 v161, v84, v85
	v_exp_f32_e32 v88, v88
	v_exp_f32_e32 v89, v89
	v_cvt_pk_fp8_f32 v160, v82, v83 op_sel:[0,0,1]
	v_cvt_pk_fp8_f32 v161, v86, v87 op_sel:[0,0,1]
	v_exp_f32_e32 v90, v90
	v_exp_f32_e32 v91, v91
	v_exp_f32_e32 v92, v92
	v_exp_f32_e32 v93, v93
	v_exp_f32_e32 v94, v94
	v_exp_f32_e32 v95, v95
	s_setprio 0
	ds_read_b128 v[80:83], v203 offset:24576
	ds_read_b128 v[212:215], v203 offset:26624
	ds_read_b128 v[84:87], v204 offset:24576
	ds_read_b128 v[216:219], v204 offset:26624
	v_cvt_pk_fp8_f32 v162, v88, v89
	v_cvt_pk_fp8_f32 v163, v92, v93
	v_exp_f32_e32 v96, v96
	v_exp_f32_e32 v97, v97
	v_cvt_pk_fp8_f32 v162, v90, v91 op_sel:[0,0,1]
	v_cvt_pk_fp8_f32 v163, v94, v95 op_sel:[0,0,1]
	v_exp_f32_e32 v98, v98
	v_exp_f32_e32 v99, v99
	v_exp_f32_e32 v100, v100
	v_exp_f32_e32 v101, v101
	v_exp_f32_e32 v102, v102
	v_exp_f32_e32 v103, v103
	v_mfma_scale_f32_32x32x64_f8f6f4 v[128:143], v[128:135], v[152:159], v[64:79], v173, v194 op_sel_hi:[0,0,0]
	v_cvt_pk_fp8_f32 v164, v96, v97
	v_cvt_pk_fp8_f32 v165, v100, v101
	v_exp_f32_e32 v104, v104
	v_exp_f32_e32 v105, v105
	v_cvt_pk_fp8_f32 v164, v98, v99 op_sel:[0,0,1]
	v_cvt_pk_fp8_f32 v165, v102, v103 op_sel:[0,0,1]
	v_exp_f32_e32 v106, v106
	v_exp_f32_e32 v107, v107
	v_exp_f32_e32 v108, v108
	v_exp_f32_e32 v109, v109
	v_exp_f32_e32 v110, v110
	v_exp_f32_e32 v111, v111
	s_nop 0
	v_cvt_pk_fp8_f32 v166, v104, v105
	v_cvt_pk_fp8_f32 v167, v108, v109
	v_cvt_pk_fp8_f32 v166, v106, v107 op_sel:[0,0,1]
	v_cvt_pk_fp8_f32 v167, v110, v111 op_sel:[0,0,1]
	s_setprio 1
	s_waitcnt lgkmcnt(0)
	v_mfma_scale_f32_32x32x64_f8f6f4 v[32:47], v[80:87], v[160:167], v[32:47], v194, v194 op_sel_hi:[0,0,0]
	v_max3_f32 v88, v112, s5, v113
	v_max3_f32 v88, v88, v114, v115
	v_max3_f32 v88, v88, v116, v117
	v_max3_f32 v88, v88, v118, v119
	v_max3_f32 v88, v88, v120, v121
	v_max3_f32 v88, v88, v122, v123
	v_max3_f32 v88, v88, v124, v125
	v_max3_f32 v88, v88, v126, v127
	v_mfma_scale_f32_32x32x64_f8f6f4 v[16:31], v[212:219], v[160:167], v[16:31], v194, v194 op_sel_hi:[0,0,0]
	v_max3_f32 v80, v128, s5, v129
	v_max3_f32 v80, v80, v130, v131
	v_max3_f32 v80, v80, v132, v133
	v_max3_f32 v80, v80, v134, v135
	v_max3_f32 v80, v80, v136, v137
	v_max3_f32 v80, v80, v138, v139
	v_max3_f32 v80, v80, v140, v141
	v_max3_f32 v80, v80, v142, v143
	v_mfma_scale_f32_32x32x64_f8f6f4 v[48:63], v[144:151], v[160:167], v[48:63], v194, v194 op_sel_hi:[0,0,0]
	s_setprio 0
	v_max_f32_e32 v80, v88, v80
	v_cmp_lt_f32_e32 vcc, s36, v80
	s_cbranch_vccnz .LBB3_15
.LBB3_11:
	s_waitcnt vmcnt(2) lgkmcnt(0)
	s_barrier
	v_add_u32_e32 v82, 0x6000, v188
	v_lshl_add_u64 v[80:81], v[176:177], 0, s[26:27]
	v_readfirstlane_b32 s6, v82
	s_mov_b32 m0, s6
	s_nop 0
	global_load_lds_dwordx4 v[80:81], off
	ds_read_b128 v[80:83], v205
	ds_read_b128 v[96:99], v205 offset:2048
	ds_read_b128 v[84:87], v206
	ds_read_b128 v[100:103], v206 offset:2048
	s_setprio 1
	v_exp_f32_e32 v112, v112
	v_exp_f32_e32 v113, v113
	v_exp_f32_e32 v114, v114
	v_exp_f32_e32 v115, v115
	v_exp_f32_e32 v116, v116
	v_exp_f32_e32 v117, v117
	v_exp_f32_e32 v118, v118
	v_exp_f32_e32 v119, v119
	s_waitcnt lgkmcnt(0)
	v_mfma_scale_f32_32x32x64_f8f6f4 v[80:95], v[80:87], v[152:159], v[64:79], v173, v194 op_sel_hi:[0,0,0]
	v_cvt_pk_fp8_f32 v160, v112, v113
	v_cvt_pk_fp8_f32 v161, v116, v117
	v_exp_f32_e32 v120, v120
	v_exp_f32_e32 v121, v121
	v_cvt_pk_fp8_f32 v160, v114, v115 op_sel:[0,0,1]
	v_cvt_pk_fp8_f32 v161, v118, v119 op_sel:[0,0,1]
	v_exp_f32_e32 v122, v122
	v_exp_f32_e32 v123, v123
	v_exp_f32_e32 v124, v124
	v_exp_f32_e32 v125, v125
	v_exp_f32_e32 v126, v126
	v_exp_f32_e32 v127, v127
	s_setprio 0
	ds_read_b128 v[112:115], v210 offset:24576
	ds_read_b128 v[212:215], v210 offset:26624
	ds_read_b128 v[116:119], v211 offset:24576
	ds_read_b128 v[216:219], v211 offset:26624
	v_cvt_pk_fp8_f32 v162, v120, v121
	v_cvt_pk_fp8_f32 v163, v124, v125
	v_exp_f32_e32 v128, v128
	v_exp_f32_e32 v129, v129
	v_cvt_pk_fp8_f32 v162, v122, v123 op_sel:[0,0,1]
	v_cvt_pk_fp8_f32 v163, v126, v127 op_sel:[0,0,1]
	v_exp_f32_e32 v130, v130
	v_exp_f32_e32 v131, v131
	v_exp_f32_e32 v132, v132
	v_exp_f32_e32 v133, v133
	v_exp_f32_e32 v134, v134
	v_exp_f32_e32 v135, v135
	v_mfma_scale_f32_32x32x64_f8f6f4 v[96:111], v[96:103], v[152:159], v[64:79], v173, v194 op_sel_hi:[0,0,0]
	v_cvt_pk_fp8_f32 v164, v128, v129
	v_cvt_pk_fp8_f32 v165, v132, v133
	v_exp_f32_e32 v136, v136
	v_exp_f32_e32 v137, v137
	v_cvt_pk_fp8_f32 v164, v130, v131 op_sel:[0,0,1]
	v_cvt_pk_fp8_f32 v165, v134, v135 op_sel:[0,0,1]
	v_exp_f32_e32 v138, v138
	v_exp_f32_e32 v139, v139
	v_exp_f32_e32 v140, v140
	v_exp_f32_e32 v141, v141
	v_exp_f32_e32 v142, v142
	v_exp_f32_e32 v143, v143
	s_nop 0
	v_cvt_pk_fp8_f32 v166, v136, v137
	v_cvt_pk_fp8_f32 v167, v140, v141
	v_cvt_pk_fp8_f32 v166, v138, v139 op_sel:[0,0,1]
	v_cvt_pk_fp8_f32 v167, v142, v143 op_sel:[0,0,1]
	s_setprio 1
	s_waitcnt lgkmcnt(0)
	v_mfma_scale_f32_32x32x64_f8f6f4 v[32:47], v[112:119], v[160:167], v[32:47], v194, v194 op_sel_hi:[0,0,0]
	v_max3_f32 v120, v80, s5, v81
	v_max3_f32 v120, v120, v82, v83
	v_max3_f32 v120, v120, v84, v85
	v_max3_f32 v120, v120, v86, v87
	v_max3_f32 v120, v120, v88, v89
	v_max3_f32 v120, v120, v90, v91
	v_max3_f32 v120, v120, v92, v93
	v_max3_f32 v120, v120, v94, v95
	v_mfma_scale_f32_32x32x64_f8f6f4 v[16:31], v[212:219], v[160:167], v[16:31], v194, v194 op_sel_hi:[0,0,0]
	v_max3_f32 v112, v96, s5, v97
	v_max3_f32 v112, v112, v98, v99
	v_max3_f32 v112, v112, v100, v101
	v_max3_f32 v112, v112, v102, v103
	v_max3_f32 v112, v112, v104, v105
	v_max3_f32 v112, v112, v106, v107
	v_max3_f32 v112, v112, v108, v109
	v_max3_f32 v112, v112, v110, v111
	v_mfma_scale_f32_32x32x64_f8f6f4 v[48:63], v[144:151], v[160:167], v[48:63], v194, v194 op_sel_hi:[0,0,0]
	s_setprio 0
	v_max_f32_e32 v112, v120, v112
	v_cmp_lt_f32_e32 vcc, s36, v112
	s_cbranch_vccnz .LBB3_16
.LBB3_12:
	s_waitcnt vmcnt(1) lgkmcnt(0)
	s_barrier
	ds_read_b128 v[112:115], v203
	ds_read_b128 v[128:131], v203 offset:2048
	ds_read_b128 v[116:119], v204
	ds_read_b128 v[132:135], v204 offset:2048
	s_setprio 1
	v_exp_f32_e32 v80, v80
	v_exp_f32_e32 v81, v81
	v_exp_f32_e32 v82, v82
	v_exp_f32_e32 v83, v83
	v_exp_f32_e32 v84, v84
	v_exp_f32_e32 v85, v85
	v_exp_f32_e32 v86, v86
	v_exp_f32_e32 v87, v87
	s_waitcnt lgkmcnt(0)
	v_mfma_scale_f32_32x32x64_f8f6f4 v[112:127], v[112:119], v[152:159], v[64:79], v173, v194 op_sel_hi:[0,0,0]
	v_cvt_pk_fp8_f32 v160, v80, v81
	v_cvt_pk_fp8_f32 v161, v84, v85
	v_exp_f32_e32 v88, v88
	v_exp_f32_e32 v89, v89
	v_cvt_pk_fp8_f32 v160, v82, v83 op_sel:[0,0,1]
	v_cvt_pk_fp8_f32 v161, v86, v87 op_sel:[0,0,1]
	v_exp_f32_e32 v90, v90
	v_exp_f32_e32 v91, v91
	v_exp_f32_e32 v92, v92
	v_exp_f32_e32 v93, v93
	v_exp_f32_e32 v94, v94
	v_exp_f32_e32 v95, v95
	s_setprio 0
	ds_read_b128 v[80:83], v205 offset:24576
	ds_read_b128 v[136:139], v205 offset:26624
	ds_read_b128 v[84:87], v206 offset:24576
	ds_read_b128 v[140:143], v206 offset:26624
	v_cvt_pk_fp8_f32 v162, v88, v89
	v_cvt_pk_fp8_f32 v163, v92, v93
	v_exp_f32_e32 v96, v96
	v_exp_f32_e32 v97, v97
	v_cvt_pk_fp8_f32 v162, v90, v91 op_sel:[0,0,1]
	v_cvt_pk_fp8_f32 v163, v94, v95 op_sel:[0,0,1]
	v_exp_f32_e32 v98, v98
	v_exp_f32_e32 v99, v99
	v_exp_f32_e32 v100, v100
	v_exp_f32_e32 v101, v101
	v_exp_f32_e32 v102, v102
	v_exp_f32_e32 v103, v103
	v_mfma_scale_f32_32x32x64_f8f6f4 v[64:79], v[128:135], v[152:159], v[64:79], v173, v194 op_sel_hi:[0,0,0]
	v_cvt_pk_fp8_f32 v164, v96, v97
	v_cvt_pk_fp8_f32 v165, v100, v101
	v_exp_f32_e32 v104, v104
	v_exp_f32_e32 v105, v105
	v_cvt_pk_fp8_f32 v164, v98, v99 op_sel:[0,0,1]
	v_cvt_pk_fp8_f32 v165, v102, v103 op_sel:[0,0,1]
	v_exp_f32_e32 v106, v106
	v_exp_f32_e32 v107, v107
	v_exp_f32_e32 v108, v108
	v_exp_f32_e32 v109, v109
	v_exp_f32_e32 v110, v110
	v_exp_f32_e32 v111, v111
	s_nop 0
	v_cvt_pk_fp8_f32 v166, v104, v105
	v_cvt_pk_fp8_f32 v167, v108, v109
	v_cvt_pk_fp8_f32 v166, v106, v107 op_sel:[0,0,1]
	v_cvt_pk_fp8_f32 v167, v110, v111 op_sel:[0,0,1]
	s_setprio 1
	s_waitcnt lgkmcnt(0)
	v_mfma_scale_f32_32x32x64_f8f6f4 v[32:47], v[80:87], v[160:167], v[32:47], v194, v194 op_sel_hi:[0,0,0]
	v_max3_f32 v88, v112, s5, v113
	v_max3_f32 v88, v88, v114, v115
	v_max3_f32 v88, v88, v116, v117
	v_max3_f32 v88, v88, v118, v119
	v_max3_f32 v88, v88, v120, v121
	v_max3_f32 v88, v88, v122, v123
	v_max3_f32 v88, v88, v124, v125
	v_max3_f32 v88, v88, v126, v127
	v_mfma_scale_f32_32x32x64_f8f6f4 v[16:31], v[136:143], v[160:167], v[16:31], v194, v194 op_sel_hi:[0,0,0]
	v_max3_f32 v80, v64, s5, v65
	v_max3_f32 v80, v80, v66, v67
	v_max3_f32 v80, v80, v68, v69
	v_max3_f32 v80, v80, v70, v71
	v_max3_f32 v80, v80, v72, v73
	v_max3_f32 v80, v80, v74, v75
	v_max3_f32 v80, v80, v76, v77
	v_max3_f32 v80, v80, v78, v79
	v_mfma_scale_f32_32x32x64_f8f6f4 v[48:63], v[144:151], v[160:167], v[48:63], v194, v194 op_sel_hi:[0,0,0]
	s_setprio 0
	v_max_f32_e32 v80, v88, v80
	v_cmp_lt_f32_e32 vcc, s36, v80
	s_cbranch_vccnz .LBB3_17

.LBB3_17:
	v_mov_b32_e32 v81, v80
	s_nop 1
	v_permlane32_swap_b32_e32 v80, v81
	v_max_f32_e32 v80, v80, v81
	v_max_f32_e32 v80, v80, v80
	v_max_f32_e32 v81, 0, v80
	v_exp_f32_e64 v80, -v81
	v_sub_f32_e32 v127, v127, v81
	v_sub_f32_e32 v126, v126, v81
	v_sub_f32_e32 v125, v125, v81
	v_sub_f32_e32 v124, v124, v81
	v_sub_f32_e32 v123, v123, v81
	v_sub_f32_e32 v122, v122, v81
	v_sub_f32_e32 v121, v121, v81
	v_sub_f32_e32 v120, v120, v81
	v_sub_f32_e32 v119, v119, v81
	v_sub_f32_e32 v118, v118, v81
	v_sub_f32_e32 v117, v117, v81
	v_sub_f32_e32 v116, v116, v81
	v_sub_f32_e32 v115, v115, v81
	v_sub_f32_e32 v114, v114, v81
	v_sub_f32_e32 v113, v113, v81
	v_sub_f32_e32 v112, v112, v81
	v_sub_f32_e32 v79, v79, v81
	v_sub_f32_e32 v78, v78, v81
	v_sub_f32_e32 v77, v77, v81
	v_sub_f32_e32 v76, v76, v81
	v_sub_f32_e32 v75, v75, v81
	v_sub_f32_e32 v74, v74, v81
	v_sub_f32_e32 v73, v73, v81
	v_sub_f32_e32 v72, v72, v81
	v_sub_f32_e32 v71, v71, v81
	v_sub_f32_e32 v70, v70, v81
	v_sub_f32_e32 v69, v69, v81
	v_sub_f32_e32 v68, v68, v81
	v_sub_f32_e32 v67, v67, v81
	v_sub_f32_e32 v66, v66, v81
	v_sub_f32_e32 v65, v65, v81
	v_sub_f32_e32 v64, v64, v81
	v_pk_mul_f32 v[46:47], v[80:81], v[46:47] op_sel_hi:[0,1]
	v_pk_mul_f32 v[44:45], v[80:81], v[44:45] op_sel_hi:[0,1]
	v_pk_mul_f32 v[42:43], v[80:81], v[42:43] op_sel_hi:[0,1]
	v_pk_mul_f32 v[40:41], v[80:81], v[40:41] op_sel_hi:[0,1]
	v_pk_mul_f32 v[38:39], v[80:81], v[38:39] op_sel_hi:[0,1]
	v_pk_mul_f32 v[36:37], v[80:81], v[36:37] op_sel_hi:[0,1]
	v_pk_mul_f32 v[34:35], v[80:81], v[34:35] op_sel_hi:[0,1]
	v_pk_mul_f32 v[32:33], v[80:81], v[32:33] op_sel_hi:[0,1]
	v_pk_mul_f32 v[30:31], v[80:81], v[30:31] op_sel_hi:[0,1]
	v_pk_mul_f32 v[28:29], v[80:81], v[28:29] op_sel_hi:[0,1]
	v_pk_mul_f32 v[26:27], v[80:81], v[26:27] op_sel_hi:[0,1]
	v_pk_mul_f32 v[24:25], v[80:81], v[24:25] op_sel_hi:[0,1]
	v_pk_mul_f32 v[22:23], v[80:81], v[22:23] op_sel_hi:[0,1]
	v_pk_mul_f32 v[20:21], v[80:81], v[20:21] op_sel_hi:[0,1]
	v_pk_mul_f32 v[18:19], v[80:81], v[18:19] op_sel_hi:[0,1]
	v_pk_mul_f32 v[16:17], v[80:81], v[16:17] op_sel_hi:[0,1]
	v_pk_mul_f32 v[62:63], v[80:81], v[62:63] op_sel_hi:[0,1]
	v_pk_mul_f32 v[60:61], v[80:81], v[60:61] op_sel_hi:[0,1]
	v_pk_mul_f32 v[58:59], v[80:81], v[58:59] op_sel_hi:[0,1]
	v_pk_mul_f32 v[56:57], v[80:81], v[56:57] op_sel_hi:[0,1]
	v_pk_mul_f32 v[54:55], v[80:81], v[54:55] op_sel_hi:[0,1]
	v_pk_mul_f32 v[52:53], v[80:81], v[52:53] op_sel_hi:[0,1]
	v_pk_mul_f32 v[50:51], v[80:81], v[50:51] op_sel_hi:[0,1]
	v_pk_mul_f32 v[48:49], v[80:81], v[48:49] op_sel_hi:[0,1]
	s_branch .LBB3_13

	.amdhsa_kernel _Z13attn11_kernelILi4EEvPc
		.amdhsa_group_segment_fixed_size 0
		.amdhsa_private_segment_fixed_size 0
		.amdhsa_kernarg_size 264
		.amdhsa_user_sgpr_count 2
		.amdhsa_user_sgpr_dispatch_ptr 0
		.amdhsa_user_sgpr_queue_ptr 0
		.amdhsa_user_sgpr_kernarg_segment_ptr 1
		.amdhsa_user_sgpr_dispatch_id 0
		.amdhsa_user_sgpr_kernarg_preload_length 0
		.amdhsa_user_sgpr_kernarg_preload_offset 0
		.amdhsa_user_sgpr_private_segment_size 0
		.amdhsa_uses_dynamic_stack 0
		.amdhsa_enable_private_segment 0
		.amdhsa_system_sgpr_workgroup_id_x 1
		.amdhsa_system_sgpr_workgroup_id_y 0
		.amdhsa_system_sgpr_workgroup_id_z 0
		.amdhsa_system_sgpr_workgroup_info 0
		.amdhsa_system_vgpr_workitem_id 0
		.amdhsa_next_free_vgpr 220
		.amdhsa_next_free_sgpr 39
		.amdhsa_accum_offset 220
		.amdhsa_reserve_vcc 1
		.amdhsa_float_round_mode_32 0
		.amdhsa_float_round_mode_16_64 0
		.amdhsa_float_denorm_mode_32 3
		.amdhsa_float_denorm_mode_16_64 3
		.amdhsa_dx10_clamp 1
		.amdhsa_ieee_mode 1
		.amdhsa_fp16_overflow 0
		.amdhsa_tg_split 0
		.amdhsa_exception_fp_ieee_invalid_op 0
		.amdhsa_exception_fp_denorm_src 0
		.amdhsa_exception_fp_ieee_div_zero 0
		.amdhsa_exception_fp_ieee_overflow 0
		.amdhsa_exception_fp_ieee_underflow 0
		.amdhsa_exception_fp_ieee_inexact 0
		.amdhsa_exception_int_div_zero 0
	.end_amdhsa_kernel
	.text
.Lfunc_end3:
	.size	_Z13attn11_kernelILi4EEvPc, .Lfunc_end3-_Z13attn11_kernelILi4EEvPc
	.set _Z13attn11_kernelILi4EEvPc.num_vgpr, 220
	.set _Z13attn11_kernelILi4EEvPc.num_agpr, 0
	.set _Z13attn11_kernelILi4EEvPc.numbered_sgpr, 39
	.set _Z13attn11_kernelILi4EEvPc.num_named_barrier, 0
	.set _Z13attn11_kernelILi4EEvPc.private_seg_size, 0
	.set _Z13attn11_kernelILi4EEvPc.uses_vcc, 1
	.set _Z13attn11_kernelILi4EEvPc.uses_flat_scratch, 0
	.set _Z13attn11_kernelILi4EEvPc.has_dyn_sized_stack, 0
	.set _Z13attn11_kernelILi4EEvPc.has_recursion, 0
	.set _Z13attn11_kernelILi4EEvPc.has_indirect_call, 0
